# MoE up/down phases: unit index uses c' = (blockIdx % 8) * 32 + blockIdx / 8 so that each XCD works on whole row blocks (its L2 fetches each gathered A row block once, as in the dense phases)
# speedup vs baseline: 1.0071x; 1.0071x over previous
.LBB0_6:
	s_ashr_i32 s3, s2, 31
	s_lshr_b32 s0, s3, 29
	s_add_i32 s5, s2, s0
	s_and_b32 s0, s5, -8
	s_sub_i32 s18, s2, s0
	s_lshl_b32 s0, s18, 4
	s_cmp_lt_i32 s18, 0
	s_mul_i32 s1, s18, 17
	s_cselect_b32 s0, s1, s0
	s_lshl_b32 s1, s18, 7
	s_cmp_lt_i32 s18, 0
	s_mul_i32 s4, s18, 0x81
	s_cselect_b32 s1, s4, s1
	s_lshl_b32 s4, s18, 6
	s_cmp_lt_i32 s18, 0
	s_movk_i32 s6, 0xc1
	s_mul_i32 s7, s18, 0x41
	s_movk_i32 s9, 0x181
	s_cselect_b32 s6, s6, 0xc0
	s_cselect_b32 s9, s9, 0x180
	s_cselect_b32 s4, s7, s4
	s_lshl_b32 s11, s2, 3
	s_lshl_b32 s7, s2, 9
	s_cmp_eq_u32 s8, 15
	v_writelane_b32 v253, s7, 6
	s_cselect_b64 s[12:13], -1, 0
	v_writelane_b32 v253, s12, 7
	s_cmp_eq_u32 s8, 14
	v_mov_b32_e32 v35, 0
	v_writelane_b32 v253, s13, 8
	s_cselect_b64 s[12:13], -1, 0
	v_writelane_b32 v253, s12, 9
	s_cmp_eq_u32 s8, 13
	s_mov_b32 s59, 0x20000
	v_writelane_b32 v253, s13, 10
	s_cselect_b64 s[12:13], -1, 0
	v_writelane_b32 v253, s12, 11
	s_cmp_eq_u32 s8, 12
	v_mbcnt_lo_u32_b32 v1, -1, 0
	v_writelane_b32 v253, s13, 12
	s_cselect_b64 s[12:13], -1, 0
	v_writelane_b32 v253, s12, 13
	s_cmp_eq_u32 s8, 11
	v_mov_b32_e32 v214, 0x358637bd
	v_writelane_b32 v253, s13, 14
	s_cselect_b64 s[12:13], -1, 0
	v_writelane_b32 v253, s12, 15
	s_cmp_eq_u32 s8, 10
	v_mov_b32_e32 v215, 1
	v_writelane_b32 v253, s13, 16
	s_cselect_b64 s[12:13], -1, 0
	v_writelane_b32 v253, s12, 17
	s_cmp_eq_u32 s8, 9
	s_movk_i32 s66, 0x4800
	v_writelane_b32 v253, s13, 18
	s_cselect_b64 s[12:13], -1, 0
	v_writelane_b32 v253, s12, 19
	s_cmp_eq_u32 s8, 8
	s_mov_b32 s67, s59
	v_writelane_b32 v253, s13, 20
	s_cselect_b64 s[12:13], -1, 0
	v_writelane_b32 v253, s12, 21
	s_cmp_eq_u32 s8, 7
	s_mov_b32 s58, 0x4f700000
	v_writelane_b32 v253, s13, 22
	s_cselect_b64 s[12:13], -1, 0
	v_writelane_b32 v253, s12, 23
	s_cmp_eq_u32 s8, 6
	v_mov_b32_e32 v216, 0x3a27c5ac
	v_writelane_b32 v253, s13, 24
	s_cselect_b64 s[12:13], -1, 0
	v_writelane_b32 v253, s12, 25
	s_cmp_eq_u32 s8, 5
	v_mov_b32_e32 v234, v35
	v_writelane_b32 v253, s13, 26
	s_cselect_b64 s[12:13], -1, 0
	v_writelane_b32 v253, s12, 27
	s_cmp_eq_u32 s8, 4
	v_mov_b32_e32 v235, v35
	v_writelane_b32 v253, s13, 28
	s_cselect_b64 s[12:13], -1, 0
	v_writelane_b32 v253, s12, 29
	s_cmp_eq_u32 s8, 3
	v_mov_b32_e32 v236, v35
	v_writelane_b32 v253, s13, 30
	s_cselect_b64 s[12:13], -1, 0
	v_writelane_b32 v253, s12, 31
	s_cmp_eq_u32 s8, 2
	v_mov_b32_e32 v237, v35
	v_writelane_b32 v253, s13, 32
	s_cselect_b64 s[12:13], -1, 0
	v_writelane_b32 v253, s12, 33
	s_cmp_eq_u32 s8, 1
	v_mov_b32_e32 v217, 2
	v_writelane_b32 v253, s13, 34
	s_cselect_b64 s[12:13], -1, 0
	v_writelane_b32 v253, s12, 35
	s_cmp_eq_u32 s8, 0
	v_mbcnt_hi_u32_b32 v218, -1, v1
	v_writelane_b32 v253, s13, 36
	s_cselect_b64 s[12:13], -1, 0
	v_writelane_b32 v253, s12, 37
	s_lshl_b32 s7, s8, 6
	s_cmpk_lt_i32 s2, 0xc00
	v_writelane_b32 v253, s13, 38
	v_writelane_b32 v253, s7, 39
	s_cselect_b64 s[12:13], -1, 0
	s_ashr_i32 s8, s5, 3
	v_writelane_b32 v253, s12, 40
	s_cmpk_lt_i32 s2, 0x600
	s_mul_i32 s5, s6, s18
	v_writelane_b32 v253, s13, 41
	s_cselect_b64 s[12:13], -1, 0
	s_add_i32 s5, s5, s8
	s_mul_hi_i32 s6, s5, 0x2aaaaaab
	s_lshr_b32 s7, s6, 31
	s_ashr_i32 s6, s6, 3
	s_add_i32 s6, s6, s7
	s_mul_i32 s7, s6, 48
	s_sub_i32 s5, s5, s7
	s_bfe_i32 s7, s5, 0x80000
	s_bfe_u32 s7, s7, 0x2000d
	s_add_i32 s7, s5, s7
	s_bfe_i32 s10, s7, 0x80000
	s_and_b32 s7, s7, 0xfc
	s_sub_i32 s5, s5, s7
	s_lshl_b32 s6, s6, 2
	s_sext_i32_i8 s5, s5
	v_writelane_b32 v253, s12, 42
	s_add_i32 s14, s6, s5
	s_mov_b32 s6, s14
	v_writelane_b32 v253, s13, 43
	s_ashr_i32 s15, s14, 31
	v_writelane_b32 v253, s6, 44
	s_sext_i32_i16 s10, s10
	s_ashr_i32 s16, s10, 4
	v_writelane_b32 v253, s7, 45
	s_lshl_b64 s[6:7], s[14:15], 19
	v_writelane_b32 v253, s6, 46
	s_lshl_b32 s5, s16, 9
	s_ashr_i32 s17, s16, 31
	v_writelane_b32 v253, s7, 47
	v_writelane_b32 v253, s5, 48
	s_ashr_i32 s5, s5, 31
	v_writelane_b32 v253, s5, 49
	s_mov_b32 s6, s16
	v_writelane_b32 v253, s6, 50
	s_ashr_i32 s12, s10, 2
	s_lshl_b32 s5, s12, 17
	v_writelane_b32 v253, s7, 51
	s_lshl_b64 s[6:7], s[16:17], 19
	v_writelane_b32 v253, s6, 52
	s_and_b32 s5, s5, 0x60000
	s_cmpk_lt_i32 s2, 0x200
	v_writelane_b32 v253, s7, 53
	v_writelane_b32 v253, s12, 54
	v_writelane_b32 v253, s5, 55
	s_cselect_b64 s[6:7], -1, 0
	v_writelane_b32 v253, s6, 56
	s_cmp_lt_i32 s2, 32
	v_mov_b64_e32 v[200:201], 0xc00
	v_writelane_b32 v253, s7, 57
	s_cselect_b64 s[6:7], -1, 0
	s_cmp_gt_i32 s2, 31
	v_writelane_b32 v253, s6, 58
	s_cselect_b64 s[12:13], -1, 0
	v_mov_b64_e32 v[202:203], 0xbff
	v_writelane_b32 v253, s7, 59
	s_and_b64 s[6:7], s[12:13], exec
	s_cselect_b32 s5, s2, 0x800
	s_bitcmp1_b32 s2, 3
	s_cselect_b64 s[6:7], -1, 0
	v_writelane_b32 v253, s12, 60
	s_and_b64 s[94:95], s[12:13], s[6:7]
	s_cmpk_lt_i32 s11, 0x4000
	v_writelane_b32 v253, s13, 61
	s_cselect_b64 s[6:7], -1, 0
	s_cmpk_lt_u32 s5, 0x800
	v_writelane_b32 v253, s11, 62
	s_cselect_b64 s[10:11], -1, 0
	s_or_b64 s[6:7], s[6:7], s[10:11]
	v_writelane_b32 v253, s5, 63
	v_writelane_b32 v254, s6, 0
	s_mul_i32 s5, s2, 0x120000
	s_lshl_b32 s80, s2, 6
	v_writelane_b32 v254, s7, 1
	s_add_i32 s6, s5, 0x3c800000
	v_writelane_b32 v254, s6, 2
	s_add_i32 s6, s5, 0x3c804800
	v_writelane_b32 v254, s6, 3
	s_add_i32 s6, s5, 0x3c809000
	v_writelane_b32 v254, s6, 4
	s_add_i32 s6, s5, 0x3c80d800
	v_writelane_b32 v254, s6, 5
	s_add_i32 s6, s5, 0x3c812000
	v_writelane_b32 v254, s6, 6
	s_add_i32 s6, s5, 0x3c816800
	v_writelane_b32 v254, s6, 7
	s_add_i32 s6, s5, 0x3c81b000
	v_writelane_b32 v254, s6, 8
	s_add_i32 s6, s5, 0x3c81f800
	v_writelane_b32 v254, s6, 9
	s_add_i32 s6, s5, 0x3c824000
	v_writelane_b32 v254, s6, 10
	s_add_i32 s5, s5, 0x3c828800
	v_writelane_b32 v254, s5, 11
	s_lshl_b32 s5, s2, 21
	s_add_i32 s6, s5, 0x307fc800
	v_writelane_b32 v254, s6, 12
	s_add_i32 s6, s5, 0x307fd800
	v_writelane_b32 v254, s6, 13
	s_add_i32 s6, s5, 0x307fe800
	v_writelane_b32 v254, s6, 14
	s_add_i32 s6, s5, 0x307ff800
	v_writelane_b32 v254, s6, 15
	s_add_i32 s6, s5, 0x30800800
	v_writelane_b32 v254, s6, 16
	s_add_i32 s6, s5, 0x30801800
	v_writelane_b32 v254, s6, 17
	s_add_i32 s6, s5, 0x30802800
	v_writelane_b32 v254, s6, 18
	s_add_i32 s6, s5, 0x30803800
	s_add_i32 s82, s5, 0x307fb800
	v_writelane_b32 v254, s6, 19
	s_add_i32 s5, s5, 0x30804800
	s_ashr_i32 s81, s80, 31
	v_writelane_b32 v254, s5, 20
	s_lshl_b64 s[6:7], s[2:3], 18
	v_writelane_b32 v254, s6, 21
	s_cmpk_lt_i32 s2, 0x400
	s_mul_i32 s5, s18, s9
	v_writelane_b32 v254, s7, 22
	s_cselect_b64 s[6:7], -1, 0
	s_bfe_u32 s19, s2, 0x10003
	v_writelane_b32 v254, s6, 23
	s_cmpk_lt_i32 s2, 0x80
	v_not_b32_e32 v219, 63
	v_writelane_b32 v254, s7, 24
	s_cselect_b64 s[6:7], -1, 0
	v_writelane_b32 v254, s6, 25
	s_cmpk_gt_i32 s2, 0x7f
	v_not_b32_e32 v220, 31
	v_writelane_b32 v254, s7, 26
	s_cselect_b64 s[6:7], -1, 0
	s_cmpk_lt_i32 s2, 0x100
	s_cselect_b64 s[10:11], -1, 0
	s_add_i32 s5, s5, s8
	v_writelane_b32 v254, s10, 27
	s_mul_hi_i32 s9, s5, 0x2aaaaaab
	s_add_i32 s4, s4, s8
	v_writelane_b32 v254, s11, 28
	s_lshr_b32 s10, s9, 31
	s_ashr_i32 s9, s9, 4
	s_add_i32 s10, s9, s10
	s_mul_i32 s9, s10, 0x60
	s_sub_i32 s5, s5, s9
	s_bfe_i32 s9, s5, 0x80000
	s_bfe_u32 s9, s9, 0x2000d
	s_add_i32 s11, s5, s9
	s_and_b32 s9, s11, 0xfc
	s_sub_i32 s5, s5, s9
	s_ashr_i32 s9, s4, 31
	s_lshr_b32 s9, s9, 28
	s_add_i32 s12, s4, s9
	s_and_b32 s9, s12, 0xfff0
	s_sub_i32 s4, s4, s9
	s_bfe_i32 s9, s4, 0x80000
	s_bfe_u32 s9, s9, 0x2000d
	s_add_i32 s13, s4, s9
	s_and_b32 s9, s13, 0xfc
	s_add_i32 s1, s1, s8
	s_sub_i32 s4, s4, s9
	s_ashr_i32 s9, s1, 31
	s_lshr_b32 s9, s9, 27
	s_add_i32 s14, s1, s9
	s_and_b32 s9, s14, 0xffe0
	s_sub_i32 s1, s1, s9
	s_bfe_i32 s9, s1, 0x80000
	s_bfe_u32 s9, s9, 0x2000d
	s_add_i32 s15, s1, s9
	s_and_b32 s9, s15, 0xfc
	s_sub_i32 s16, s1, s9
	s_lshr_b32 s1, s3, 30
	s_add_i32 s1, s2, s1
	s_ashr_i32 s9, s1, 2
	v_writelane_b32 v254, s9, 29
	s_add_i32 s9, 0, 0x20000
	s_lshl_b32 s17, s8, 2
	s_and_b32 s1, s1, -4
	s_add_i32 s17, s9, s17
	v_writelane_b32 v254, s17, 30
	s_add_i32 s9, s9, s1
	v_writelane_b32 v254, s9, 31
	s_ashr_i32 s9, s8, 31
	s_sub_i32 s24, s2, s1
	s_add_i32 s26, s0, s8
	s_lshl_b64 s[0:1], s[8:9], 18
	v_writelane_b32 v254, s0, 32
	s_sext_i32_i8 s5, s5
	s_sext_i32_i8 s4, s4
	v_writelane_b32 v254, s1, 33
	s_bfe_i32 s1, s11, 0x80000
	s_lshl_b32 s0, s10, 2
	s_sext_i32_i16 s1, s1
	s_add_i32 s20, s0, s5
	s_ashr_i32 s0, s1, 2
	v_writelane_b32 v254, s0, 34
	s_lshr_b32 s0, s1, 2
	s_bfe_i64 s[0:1], s[0:1], 0x100000
	s_lshl_b64 s[0:1], s[0:1], 20
	v_writelane_b32 v254, s0, 35
	s_ashr_i32 s25, s24, 31
	s_mov_b32 s8, s19
	v_writelane_b32 v254, s1, 36
	s_ashr_i32 s0, s12, 4
	s_bfe_i32 s1, s13, 0x80000
	s_lshl_b32 s0, s0, 2
	s_sext_i32_i16 s1, s1
	s_add_i32 s22, s0, s4
	s_lshr_b32 s0, s1, 2
	s_ashr_i32 s5, s1, 2
	s_bfe_i64 s[0:1], s[0:1], 0x100000
	s_lshl_b64 s[0:1], s[0:1], 17
	v_writelane_b32 v254, s0, 37
	s_sext_i32_i8 s4, s16
	s_ashr_i32 s19, s18, 31
	v_writelane_b32 v254, s1, 38
	s_ashr_i32 s0, s14, 5
	s_bfe_i32 s1, s15, 0x80000
	s_lshl_b32 s0, s0, 2
	s_sext_i32_i16 s1, s1
	s_add_i32 s88, s0, s4
	s_lshr_b32 s0, s1, 2
	s_ashr_i32 s83, s1, 2
	s_bfe_i64 s[0:1], s[0:1], 0x100000
	s_lshl_b64 s[14:15], s[0:1], 19
	v_writelane_b32 v254, s14, 39
	s_lshl_b64 s[0:1], s[0:1], 20
	s_ashr_i32 s21, s20, 31
	v_writelane_b32 v254, s15, 40
	v_writelane_b32 v254, s0, 41
	s_ashr_i32 s23, s22, 31
	s_ashr_i32 s89, s88, 31
	v_writelane_b32 v254, s1, 42
	v_writelane_b32 v254, s5, 43
	s_lshl_b32 s0, s5, 9
	v_writelane_b32 v254, s0, 44
	s_ashr_i32 s0, s0, 31
	v_writelane_b32 v254, s0, 45
	s_mov_b32 s0, s24
	v_writelane_b32 v254, s0, 46
	s_ashr_i32 s27, s26, 31
	v_mov_b32_e32 v221, 0x7fc00000
	v_writelane_b32 v254, s1, 47
	s_lshl_b64 s[0:1], s[24:25], 20
	v_writelane_b32 v254, s0, 48
	v_mov_b32_e32 v222, 0x80
	v_mov_b32_e32 v223, 0xff800000
	v_writelane_b32 v254, s1, 49
	s_mov_b32 s0, s18
	v_writelane_b32 v254, s0, 50
	v_mov_b64_e32 v[204:205], 0x400
	v_mov_b64_e32 v[206:207], 0x3ff
	v_writelane_b32 v254, s1, 51
	s_lshl_b64 s[0:1], s[18:19], 18
	v_writelane_b32 v254, s0, 52
	v_mov_b64_e32 v[210:211], 0x7f
	s_movk_i32 s33, 0xc0
	v_writelane_b32 v254, s1, 53
	s_and_b32 s96, s2, 7
	s_lshl_b32 s96, s96, 5
	s_lshr_b32 s97, s2, 3
	s_or_b32 s96, s96, s97
	v_writelane_b32 v252, s96, 47
	s_lshr_b32 s97, s96, 2
	v_writelane_b32 v254, s97, 29
	s_and_b32 s97, s96, -4
	s_add_i32 s97, s97, 0x20000
	v_writelane_b32 v254, s97, 31
	s_and_b32 s97, s96, 3
	v_writelane_b32 v254, s97, 46
	s_lshl_b32 s97, s97, 20
	v_writelane_b32 v254, s97, 48
	s_lshr_b32 s97, s96, 3
	s_lshl_b32 s97, s97, 2
	s_add_i32 s97, s97, 0x20000
	v_writelane_b32 v254, s97, 30
	s_lshr_b32 s97, s96, 3
	s_lshl_b32 s97, s97, 18
	v_writelane_b32 v254, s97, 32
	s_and_b32 s97, s96, 7
	v_writelane_b32 v254, s97, 50
	s_lshl_b32 s97, s97, 18
	v_writelane_b32 v254, s97, 52
	s_mov_b32 s97, 0
	v_writelane_b32 v254, s97, 47
	v_writelane_b32 v254, s97, 49
	v_writelane_b32 v254, s97, 51
	v_writelane_b32 v254, s97, 53
	v_writelane_b32 v254, s97, 33
	s_mov_b32 s0, s20
	v_writelane_b32 v254, s0, 54
	s_movk_i32 s72, 0x7fff
	s_movk_i32 s73, 0x1000
	v_writelane_b32 v254, s1, 55
	s_lshl_b64 s[0:1], s[20:21], 20
	v_writelane_b32 v254, s0, 56
	s_movk_i32 s90, 0x2000
	s_movk_i32 s91, 0x3000
	v_writelane_b32 v254, s1, 57
	s_mov_b32 s0, s22
	v_writelane_b32 v254, s0, 58
	s_mov_b32 s92, 0x34800000
	s_mov_b32 s97, 0
	v_writelane_b32 v254, s1, 59
	s_lshl_b64 s[0:1], s[22:23], 19
	v_writelane_b32 v254, s0, 60
	s_mov_b64 s[78:79], 0x80
	s_mov_b64 s[76:77], 0x8000000
	v_writelane_b32 v254, s1, 61
	s_lshl_b64 s[0:1], s[88:89], 19
	v_writelane_b32 v254, s0, 62
	s_nop 1
	v_writelane_b32 v254, s1, 63
	s_lshl_b64 s[0:1], s[88:89], 20
	v_writelane_b32 v252, s0, 0
	s_nop 1
	v_writelane_b32 v252, s1, 1
	s_mov_b32 s0, s26
	v_writelane_b32 v252, s0, 2
	s_nop 1
	v_writelane_b32 v252, s1, 3
	s_lshl_b64 s[0:1], s[26:27], 20
	v_writelane_b32 v252, s0, 4
	s_nop 1
	v_writelane_b32 v252, s1, 5
	s_xor_b64 s[0:1], s[94:95], -1
	v_writelane_b32 v252, s0, 6
	s_nop 1
	v_writelane_b32 v252, s1, 7
	s_add_u32 s0, s60, 0x1000
	v_writelane_b32 v252, s0, 8
	s_addc_u32 s0, s61, 0
	v_writelane_b32 v252, s0, 9
	s_xor_b64 s[0:1], s[6:7], -1
	v_writelane_b32 v252, s0, 10
	s_add_i32 s4, 0, 0x20600
	s_mov_b32 s6, 0x3ffff
	v_writelane_b32 v252, s1, 11
	s_lshl_b32 s0, s2, 4
	v_writelane_b32 v252, s0, 12
	s_lshl_b32 s0, s2, 7
	v_writelane_b32 v252, s0, 13
	s_or_b32 s0, s0, 1
	v_writelane_b32 v252, s0, 14
	s_lshl_b32 s0, s2, 5
	v_writelane_b32 v252, s0, 15
	s_lshl_b32 s0, s2, 8
	v_writelane_b32 v252, s0, 16
	s_add_i32 s0, 0, 0x24020
	v_writelane_b32 v252, s0, 17
	s_add_i32 s0, 0, 0x24024
	v_writelane_b32 v252, s0, 18
	v_writelane_b32 v252, s4, 19
	s_add_i32 s4, 0, 0x20800
	v_writelane_b32 v252, s4, 20
	s_add_i32 s4, 0, 0x20a00
	v_writelane_b32 v252, s4, 21
	s_lshl_b64 s[4:5], s[80:81], 2
	v_writelane_b32 v252, s4, 22
	s_mov_b32 s0, 0x24800000
	s_mov_b32 s1, 0x2c800000
	v_writelane_b32 v252, s5, 23
	s_load_dwordx2 s[4:5], s[84:85], 0x100
	v_writelane_b32 v252, s84, 24
	s_waitcnt lgkmcnt(0)
	s_mov_b32 s48, s4
	v_writelane_b32 v252, s85, 25
	v_writelane_b32 v252, s93, 26
	v_writelane_b32 v252, s86, 27
	s_nop 1
	v_writelane_b32 v252, s87, 28
	v_writelane_b32 v252, s80, 29
	s_nop 1
	v_writelane_b32 v252, s81, 30
	v_writelane_b32 v252, s82, 31
	v_writelane_b32 v252, s88, 32
	s_nop 1
	v_writelane_b32 v252, s89, 33
	v_writelane_b32 v252, s83, 34
	s_branch .LBB0_8

.LBB0_1079:
	s_or_b64 exec, exec, s[4:5]
	v_readlane_b32 s4, v252, 19
	s_waitcnt lgkmcnt(0)
	s_barrier
	v_mov_b32_e32 v1, s4
	ds_read_b32 v1, v1
	s_add_u32 s4, s18, 0x45000000
	s_movk_i32 s6, 0x100
	s_addc_u32 s5, s19, 0
	v_cmp_gt_i32_e64 s[40:41], s6, v164
	s_waitcnt lgkmcnt(0)
	v_readfirstlane_b32 s14, v1
	s_lshl_b32 s20, s14, 2
	v_lshlrev_b32_e32 v1, 2, v164
	v_readlane_b32 s6, v252, 20
	s_ashr_i32 s21, s20, 31
	s_ashr_i32 s26, s46, 31
	v_add_u32_e32 v6, s6, v1
	v_readlane_b32 s14, v252, 47
	s_mov_b32 s15, 0
	s_branch .LBB0_1083

.LBB0_1087:
	s_add_u32 s44, s18, 0x24800000
	s_addc_u32 s45, s19, 0
	v_mov_b32_e32 v2, v0
	s_waitcnt lgkmcnt(0)
	s_barrier
	v_readlane_b32 s96, v252, 47
	s_nop 1
	s_cmp_ge_i32 s96, s20
	v_readfirstlane_b32 s4, v2
	s_cbranch_scc1 .LBB0_1105
	v_bfe_i32 v5, v2, 27, 1
	v_lshlrev_b32_e32 v3, 4, v2
	v_lshrrev_b32_e32 v5, 22, v5
	v_add_u32_e32 v5, v3, v5
	v_and_b32_e32 v5, 0xfffffc00, v5
	v_sub_u32_e32 v5, v3, v5
	v_ashrrev_i32_e32 v4, 31, v2
	v_lshrrev_b32_e32 v6, 4, v5
	v_lshrrev_b32_e32 v4, 26, v4
	v_bitop3_b32 v5, v6, v5, 32 bitop3:0x6c
	v_add_u32_e32 v4, v2, v4
	v_ashrrev_i32_e32 v7, 31, v5
	v_ashrrev_i32_e32 v4, 6, v4
	v_lshrrev_b32_e32 v7, 26, v7
	v_lshlrev_b32_e32 v6, 3, v4
	v_add_u32_e32 v7, v5, v7
	v_and_b32_e32 v6, -16, v6
	v_ashrrev_i32_e32 v8, 6, v7
	v_add_u32_e32 v165, v8, v6
	v_and_b32_e32 v6, 0xc0, v7
	v_sub_u32_e32 v5, v5, v6
	v_lshlrev_b32_e32 v4, 5, v4
	v_ashrrev_i16_sdwa v5, v215, sext(v5) dst_sel:DWORD dst_unused:UNUSED_PAD src0_sel:DWORD src1_sel:BYTE_0
	v_and_b32_e32 v4, 32, v4
	v_bfe_i32 v5, v5, 0, 16
	v_add_u32_e32 v3, 0x2000, v3
	v_add_lshl_u32 v176, v4, v5, 1
	v_ashrrev_i32_e32 v4, 31, v3
	v_lshrrev_b32_e32 v4, 22, v4
	v_add_u32_e32 v4, v3, v4
	v_ashrrev_i32_e32 v4, 10, v4
	v_mul_i32_i24_e32 v5, 0x400, v4
	v_sub_u32_e32 v3, v3, v5
	v_lshrrev_b32_e32 v5, 4, v3
	v_bitop3_b32 v3, v5, v3, 32 bitop3:0x6c
	v_ashrrev_i32_e32 v6, 31, v3
	v_lshrrev_b32_e32 v6, 26, v6
	v_lshlrev_b32_e32 v5, 3, v4
	v_add_u32_e32 v6, v3, v6
	v_and_b32_e32 v5, -16, v5
	v_ashrrev_i32_e32 v7, 6, v6
	v_add_u32_e32 v177, v7, v5
	v_and_b32_e32 v5, 0xc0, v6
	v_sub_u32_e32 v3, v3, v5
	v_lshlrev_b32_e32 v4, 5, v4
	v_ashrrev_i16_sdwa v3, v215, sext(v3) dst_sel:DWORD dst_unused:UNUSED_PAD src0_sel:DWORD src1_sel:BYTE_0
	v_and_b32_e32 v4, 32, v4
	v_bfe_i32 v3, v3, 0, 16
	v_add_lshl_u32 v178, v4, v3, 1
	v_and_b32_e32 v3, 3, v7
	s_mov_b32 s6, 0xfffe0
	v_lshrrev_b32_e32 v4, 2, v177
	v_lshlrev_b32_e32 v5, 1, v177
	v_and_or_b32 v3, v177, s6, v3
	v_and_b32_e32 v4, 4, v4
	v_and_b32_e32 v5, 24, v5
	v_or3_b32 v3, v3, v4, v5
	v_lshl_add_u32 v166, v3, 12, v178
	v_and_b32_e32 v3, 3, v8
	v_and_or_b32 v3, v165, s6, v3
	v_readlane_b32 s6, v254, 31
	s_ashr_i32 s14, s4, 6
	s_ashr_i32 s5, s4, 8
	v_mov_b32_e32 v5, s6
	ds_read_b32 v5, v5
	s_lshl_b32 s21, s14, 10
	s_add_u32 s22, s18, 0x4800000
	s_addc_u32 s23, s19, 0
	v_lshrrev_b32_e32 v4, 2, v165
	s_waitcnt lgkmcnt(0)
	v_readfirstlane_b32 s24, v5
	s_ashr_i32 s25, s24, 31
	s_lshl_b64 s[24:25], s[24:25], 22
	s_add_u32 s15, s44, s24
	v_lshlrev_b32_e32 v6, 1, v165
	s_addc_u32 s24, s45, s25
	v_readlane_b32 s6, v254, 48
	v_and_b32_e32 v4, 4, v4
	v_and_b32_e32 v6, 24, v6
	v_readlane_b32 s7, v254, 49
	s_add_u32 s40, s15, s6
	v_or3_b32 v3, v3, v4, v6
	s_addc_u32 s41, s24, s7
	v_lshlrev_b32_e32 v4, 2, v165
	v_readlane_b32 s6, v252, 20
	v_lshlrev_b32_e32 v6, 2, v177
	s_add_i32 s48, s21, 0
	s_mov_b64 s[42:43], s[22:23]
	v_add_u32_e32 v5, s6, v4
	v_add_u32_e32 v7, s6, v6
	v_readlane_b32 s6, v252, 21
	s_add_i32 s49, s48, 0x10000
	s_add_i32 s50, s48, 0x12000
	v_add_u32_e32 v4, s6, v4
	v_add_u32_e32 v6, s6, v6
	v_lshl_add_u32 v168, v3, 12, v176
	s_mov_b32 m0, s49
	s_add_u32 s24, s40, 0x80000
	ds_read_b32 v5, v5
	ds_read_b32 v7, v7
	ds_read_b32 v4, v4
	ds_read_b32 v6, v6
	global_load_lds_dwordx4 v168, s[40:41]
	s_mov_b32 m0, s50
	s_addc_u32 s25, s41, 0
	s_add_i32 s51, s48, 0x14000
	global_load_lds_dwordx4 v166, s[40:41]
	s_mov_b32 m0, s51
	s_add_i32 s52, s48, 0x16000
	global_load_lds_dwordx4 v168, s[24:25]
	s_mov_b32 m0, s52
	s_waitcnt lgkmcnt(0)
	v_lshl_add_u32 v34, v5, 12, v176
	global_load_lds_dwordx4 v166, s[24:25]
	s_mov_b32 m0, s48
	s_add_i32 s53, s48, 0x2000
	v_lshl_add_u32 v170, v7, 12, v178
	global_load_lds_dwordx4 v34, s[42:43]
	s_mov_b32 m0, s53
	s_add_i32 s54, s48, 0x4000
	v_lshl_add_u32 v172, v4, 12, v176
	global_load_lds_dwordx4 v170, s[42:43]
	s_mov_b32 m0, s54
	s_add_i32 s55, s48, 0x6000
	v_lshl_add_u32 v174, v6, 12, v178
	global_load_lds_dwordx4 v172, s[42:43]
	s_mov_b32 m0, s55
	s_cmp_eq_u32 s5, 1
	global_load_lds_dwordx4 v174, s[42:43]
	s_cselect_b64 s[24:25], -1, 0
	s_cmp_lg_u32 s5, 1
	s_cbranch_scc1 .LBB0_1090
	s_barrier

.LBB0_1093:
	s_add_i32 s64, s64, 1
	s_mul_i32 s4, s64, s46
	v_readlane_b32 s96, v252, 47
	s_nop 1
	s_add_i32 s4, s4, s96
	s_cmp_lt_i32 s4, s20
	s_cselect_b64 s[36:37], -1, 0
	s_cmp_ge_i32 s4, s20
	s_cbranch_scc1 .LBB0_1095
	s_ashr_i32 s5, s4, 31
	s_lshr_b32 s5, s5, 30
	s_add_i32 s5, s4, s5
	s_ashr_i32 s65, s5, 2
	s_and_b32 s5, s5, -4
	s_sub_i32 s30, s4, s5
	s_add_i32 s4, s5, 0
	s_add_i32 s4, s4, 0x20000
	v_mov_b32_e32 v2, s4
	ds_read_b32 v2, v2
	s_mov_b64 s[38:39], s[22:23]
	s_waitcnt lgkmcnt(0)
	v_readfirstlane_b32 s4, v2
	s_ashr_i32 s5, s4, 31
	s_lshl_b64 s[4:5], s[4:5], 22
	s_add_u32 s14, s44, s4
	s_addc_u32 s15, s45, s5
	s_ashr_i32 s31, s30, 31
	s_lshl_b64 s[4:5], s[30:31], 20
	s_add_u32 s34, s14, s4
	s_addc_u32 s35, s15, s5
	s_mov_b32 s31, s64

.LBB0_1105:
	s_abs_i32 s4, s46
	v_cvt_f32_u32_e32 v2, s4
	s_ashr_i32 s5, s20, 31
	s_abs_i32 s14, s20
	s_sub_i32 s15, 0, s4
	v_rcp_iflag_f32_e32 v2, v2
	s_nop 0
	v_mul_f32_e32 v2, 0x4f7ffffe, v2
	v_cvt_u32_f32_e32 v2, v2
	s_nop 0
	v_readfirstlane_b32 s20, v2
	s_mul_i32 s15, s15, s20
	s_mul_hi_u32 s15, s20, s15
	s_add_i32 s20, s20, s15
	s_mul_hi_u32 s15, s14, s20
	s_mul_i32 s15, s15, s4
	s_sub_i32 s14, s14, s15
	s_sub_i32 s15, s14, s4
	s_cmp_ge_u32 s14, s4
	s_cselect_b32 s14, s15, s14
	s_sub_i32 s15, s14, s4
	s_cmp_ge_u32 s14, s4
	s_cselect_b32 s4, s15, s14
	s_xor_b32 s4, s4, s5
	s_sub_i32 s22, s4, s5
	v_readlane_b32 s96, v252, 47
	s_nop 1
	s_cmp_lt_i32 s96, s22
	s_cbranch_scc1 .LBB0_1122
	s_sub_i32 s15, s96, s22
	s_ashr_i32 s5, s47, 6
	s_lshl_b32 s23, s15, 3
	s_add_i32 s23, s23, s5
	s_mov_b32 s20, 27
	s_mov_b32 s14, 28
	s_mov_b32 s4, 29
	s_cmpk_gt_i32 s23, 0x3fff
	s_cbranch_scc1 .LBB0_1122
	s_add_u32 s40, s18, 0x2c800000
	s_addc_u32 s41, s19, 0
	s_ashr_i32 s21, s20, 31
	s_lshl_b64 s[18:19], s[20:21], 3
	s_add_u32 s18, s84, s18
	s_addc_u32 s19, s85, s19
	s_load_dwordx2 s[18:19], s[18:19], 0x0
	s_lshl_b64 s[16:17], s[16:17], 2
	v_and_b32_e32 v36, 56, v164
	v_and_b32_e32 v38, 28, v1
	s_waitcnt lgkmcnt(0)
	s_add_u32 s42, s18, s16
	s_addc_u32 s43, s19, s17
	s_ashr_i32 s15, s14, 31
	s_lshl_b64 s[14:15], s[14:15], 3
	s_add_u32 s14, s84, s14
	s_addc_u32 s15, s85, s15
	s_load_dwordx2 s[14:15], s[14:15], 0x0
	s_waitcnt lgkmcnt(0)
	s_add_u32 s47, s14, s16
	s_addc_u32 s48, s15, s17
	s_ashr_i32 s5, s4, 31
	s_lshl_b64 s[4:5], s[4:5], 3
	s_add_u32 s4, s84, s4
	s_addc_u32 s5, s85, s5
	s_load_dwordx2 s[4:5], s[4:5], 0x0
	s_waitcnt lgkmcnt(0)
	s_add_u32 s49, s4, s16
	s_addc_u32 s50, s5, s17
	s_sub_i32 s4, s46, s22
	s_add_i32 s46, s23, 0x8000
	s_lshl_b32 s51, s4, 3
	s_lshl_b32 s52, s4, 4
	s_branch .LBB0_1109

.LBB0_1182:
	s_or_b64 exec, exec, s[4:5]
	v_readlane_b32 s4, v252, 19
	s_waitcnt lgkmcnt(0)
	s_barrier
	v_mov_b32_e32 v1, s4
	ds_read_b32 v1, v1
	s_add_u32 s4, s20, 0x45000000
	s_movk_i32 s6, 0x100
	s_addc_u32 s5, s21, 0
	v_cmp_gt_i32_e64 s[40:41], s6, v2
	s_waitcnt lgkmcnt(0)
	v_readfirstlane_b32 s14, v1
	s_lshl_b32 s16, s14, 3
	v_readlane_b32 s6, v252, 20
	s_ashr_i32 s17, s16, 31
	s_ashr_i32 s24, s38, 31
	v_lshl_add_u32 v1, v2, 2, s6
	v_readlane_b32 s14, v252, 47
	s_mov_b32 s15, 0
	s_mov_b32 s6, 0x3ffff
	s_branch .LBB0_1186

.LBB0_1190:
	v_mov_b32_e32 v1, v0
	s_waitcnt lgkmcnt(0)
	s_barrier
	v_readlane_b32 s96, v252, 47
	s_nop 1
	s_cmp_ge_i32 s96, s16
	v_readfirstlane_b32 s4, v1
	s_cbranch_scc1 .LBB0_1222
	v_lshlrev_b32_e32 v2, 4, v1
	v_add_u32_e32 v3, 0x2000, v2
	v_ashrrev_i32_e32 v4, 31, v3
	v_lshrrev_b32_e32 v4, 22, v4
	v_add_u32_e32 v4, v3, v4
	v_ashrrev_i32_e32 v10, 10, v4
	v_mul_i32_i24_e32 v4, 0x400, v10
	v_sub_u32_e32 v3, v3, v4
	v_lshrrev_b32_e32 v4, 4, v3
	v_bitop3_b32 v3, v4, v3, 32 bitop3:0x6c
	v_ashrrev_i32_e32 v4, 31, v3
	v_lshrrev_b32_e32 v4, 26, v4
	v_add_u32_e32 v4, v3, v4
	v_lshlrev_b32_e32 v5, 3, v10
	v_ashrrev_i32_e32 v11, 6, v4
	v_and_b32_e32 v5, -16, v5
	v_add_u32_e32 v5, v11, v5
	v_and_b32_e32 v6, 3, v11
	s_mov_b32 s6, 0x3fffe0
	v_lshrrev_b32_e32 v7, 2, v5
	v_lshlrev_b32_e32 v8, 1, v5
	v_and_b32_e32 v4, 0xc0, v4
	v_and_or_b32 v6, v5, s6, v6
	v_and_b32_e32 v7, 4, v7
	v_and_b32_e32 v8, 24, v8
	v_sub_u32_e32 v3, v3, v4
	v_or3_b32 v6, v6, v7, v8
	v_lshlrev_b32_e32 v7, 5, v10
	v_ashrrev_i16_sdwa v3, v215, sext(v3) dst_sel:DWORD dst_unused:UNUSED_PAD src0_sel:DWORD src1_sel:BYTE_0
	v_and_b32_e32 v7, 32, v7
	v_bfe_i32 v12, v3, 0, 16
	v_add_lshl_u32 v3, v7, v12, 1
	v_lshl_add_u32 v132, v6, 10, v3
	v_lshl_add_u32 v134, v5, 10, v3
	v_bfe_i32 v3, v1, 27, 1
	v_lshrrev_b32_e32 v3, 22, v3
	v_add_u32_e32 v3, v2, v3
	v_and_b32_e32 v3, 0xfffffc00, v3
	v_sub_u32_e32 v2, v2, v3
	v_lshrrev_b32_e32 v3, 4, v2
	v_ashrrev_i32_e32 v4, 31, v1
	v_bitop3_b32 v2, v3, v2, 32 bitop3:0x6c
	v_lshrrev_b32_e32 v4, 26, v4
	v_ashrrev_i32_e32 v3, 31, v2
	v_add_u32_e32 v4, v1, v4
	v_lshrrev_b32_e32 v3, 26, v3
	v_ashrrev_i32_e32 v14, 6, v4
	v_add_u32_e32 v3, v2, v3
	v_lshlrev_b32_e32 v4, 3, v14
	v_ashrrev_i32_e32 v13, 6, v3
	v_and_b32_e32 v4, -16, v4
	v_and_b32_e32 v3, 0xc0, v3
	v_add_u32_e32 v4, v13, v4
	v_and_b32_e32 v5, 3, v13
	v_sub_u32_e32 v2, v2, v3
	v_and_or_b32 v5, v4, s6, v5
	v_ashrrev_i16_sdwa v2, v215, sext(v2) dst_sel:DWORD dst_unused:UNUSED_PAD src0_sel:DWORD src1_sel:BYTE_0
	v_readlane_b32 s6, v254, 30
	s_ashr_i32 s5, s4, 6
	v_bfe_i32 v15, v2, 0, 16
	v_mov_b32_e32 v2, s6
	s_ashr_i32 s22, s4, 8
	s_lshl_b32 s14, s5, 10
	ds_read_b32 v2, v2
	s_add_u32 s15, s20, 0xc800000
	s_addc_u32 s17, s21, 0
	s_add_u32 s39, s20, 0x2c800000
	s_addc_u32 s40, s21, 0
	v_readlane_b32 s6, v254, 32
	s_waitcnt lgkmcnt(0)
	v_readfirstlane_b32 s18, v2
	v_readlane_b32 s7, v254, 33
	s_add_u32 s34, s15, s6
	s_addc_u32 s35, s17, s7
	s_ashr_i32 s19, s18, 31
	v_lshrrev_b32_e32 v6, 2, v4
	v_lshlrev_b32_e32 v7, 1, v4
	s_lshl_b64 s[18:19], s[18:19], 21
	v_and_b32_e32 v6, 4, v6
	v_and_b32_e32 v7, 24, v7
	s_add_u32 s18, s39, s18
	v_or3_b32 v5, v5, v6, v7
	v_lshlrev_b32_e32 v6, 5, v14
	s_addc_u32 s19, s40, s19
	v_readlane_b32 s6, v254, 52
	v_and_b32_e32 v6, 32, v6
	v_readlane_b32 s7, v254, 53
	s_add_u32 s36, s18, s6
	v_add_lshl_u32 v3, v6, v15, 1
	s_addc_u32 s37, s19, s7
	s_add_i32 s41, s14, 0
	v_lshl_add_u32 v138, v5, 10, v3
	s_add_i32 m0, s41, 0x10000
	v_lshl_add_u32 v140, v4, 10, v3
	global_load_lds_dwordx4 v138, s[36:37]
	s_add_i32 m0, s41, 0x12000
	s_add_u32 s18, s36, 0x20000
	global_load_lds_dwordx4 v132, s[36:37]
	s_addc_u32 s19, s37, 0
	s_add_i32 m0, s41, 0x14000
	s_add_i32 s42, s41, 0x2000
	global_load_lds_dwordx4 v138, s[18:19]
	s_add_i32 m0, s41, 0x16000
	s_add_i32 s43, s41, 0x4000
	global_load_lds_dwordx4 v132, s[18:19]
	s_mov_b32 m0, s41
	v_add_u32_e32 v142, 0x20000, v140
	global_load_lds_dwordx4 v140, s[34:35]
	s_mov_b32 m0, s42
	s_add_i32 s44, s41, 0x6000
	global_load_lds_dwordx4 v134, s[34:35]
	s_mov_b32 m0, s43
	v_add_u32_e32 v136, 0x20000, v134
	global_load_lds_dwordx4 v142, s[34:35]
	s_mov_b32 m0, s44
	v_mov_b32_e32 v139, v35
	global_load_lds_dwordx4 v136, s[34:35]
	v_mov_b32_e32 v133, v35
	v_mov_b32_e32 v141, v35
	v_mov_b32_e32 v135, v35
	s_cmp_eq_u32 s22, 1
	v_lshl_add_u64 v[8:9], s[36:37], 0, v[138:139]
	v_lshl_add_u64 v[6:7], s[36:37], 0, v[132:133]
	v_lshl_add_u64 v[2:3], s[34:35], 0, v[140:141]
	s_cselect_b64 s[18:19], -1, 0
	s_cmp_lg_u32 s22, 1
	v_lshl_add_u64 v[4:5], s[34:35], 0, v[134:135]
	s_cbranch_scc1 .LBB0_1193
	s_barrier

.LBB0_1196:
	s_add_i32 s47, s47, 1
	s_mul_i32 s4, s47, s38
	v_readlane_b32 s96, v252, 47
	s_nop 1
	s_add_i32 s4, s4, s96
	s_cmp_lt_i32 s4, s16
	s_cselect_b64 s[30:31], -1, 0
	s_cmp_ge_i32 s4, s16
	s_cbranch_scc1 .LBB0_1198
	s_ashr_i32 s5, s4, 31
	s_lshr_b32 s5, s5, 29
	s_add_i32 s5, s4, s5
	s_ashr_i32 s26, s5, 3
	s_lshl_b32 s24, s26, 2
	s_add_i32 s24, s24, 0
	s_add_i32 s24, s24, 0x20000
	v_mov_b32_e32 v2, s24
	ds_read_b32 v2, v2
	s_and_b32 s5, s5, -8
	s_ashr_i32 s27, s26, 31
	s_sub_i32 s24, s4, s5
	s_lshl_b64 s[4:5], s[26:27], 18
	s_waitcnt lgkmcnt(0)
	v_readfirstlane_b32 s28, v2
	s_add_u32 s26, s15, s4
	s_addc_u32 s27, s17, s5
	s_ashr_i32 s29, s28, 31
	s_lshl_b64 s[4:5], s[28:29], 21
	s_add_u32 s28, s39, s4
	s_addc_u32 s29, s40, s5
	s_ashr_i32 s25, s24, 31
	s_lshl_b64 s[4:5], s[24:25], 18
	s_add_u32 s28, s28, s4
	s_addc_u32 s29, s29, s5
	s_mov_b32 s25, s47
